# speedup vs baseline: 1.0180x; 1.0046x over previous
_Z13expert_kernelPKcPKfPKiPK15HIP_vector_typeIiLj4EES4_Pf:
	s_load_dwordx2 s[4:5], s[0:1], 0x18
	s_mov_b32 s3, 0
	s_lshr_b32 s8, s2, 2
	s_mov_b32 s9, s3
	s_lshl_b64 s[6:7], s[8:9], 4
	s_waitcnt lgkmcnt(0)
	s_add_u32 s4, s4, s6
	s_addc_u32 s5, s5, s7
	s_load_dword s6, s[4:5], 0x8
	s_waitcnt lgkmcnt(0)
	s_cmp_eq_u32 s6, 0
	s_cbranch_scc1 .LBB3_8
	s_load_dwordx2 s[12:13], s[4:5], 0x0
	s_load_dwordx2 s[10:11], s[0:1], 0x10
	v_and_b32_e32 v6, 31, v0
	s_add_i32 s6, s6, -1
	v_min_i32_e32 v1, s6, v6
	s_waitcnt lgkmcnt(0)
	v_add_u32_e32 v2, s13, v1
	v_ashrrev_i32_e32 v3, 31, v2
	v_lshl_add_u64 v[2:3], v[2:3], 2, s[10:11]
	global_load_dword v89, v[2:3], off
	s_load_dwordx4 s[4:7], s[0:1], 0x0
	s_load_dwordx2 s[10:11], s[0:1], 0x28
	v_lshrrev_b32_e32 v7, 6, v0
	s_and_b32 s9, s2, 3
	v_lshlrev_b32_e32 v8, 7, v7
	v_mov_b32_e32 v5, 0
	v_lshlrev_b32_e32 v9, 2, v6
	v_lshl_or_b32 v12, s9, 9, v8
	v_cmp_gt_u32_e32 vcc, 25, v6
	v_lshlrev_b32_e32 v8, 8, v12
	v_bfe_u32 v1, v0, 5, 1
	v_cndmask_b32_e32 v13, 0, v9, vcc
	v_mov_b32_e32 v9, v5
	v_lshlrev_b32_e32 v2, 4, v1
	v_mov_b32_e32 v3, v5
	v_accvgpr_write_b32 a63, 0
	v_accvgpr_write_b32 a62, 0
	v_accvgpr_write_b32 a61, 0
	v_accvgpr_write_b32 a60, 0
	v_accvgpr_write_b32 a59, 0
	v_accvgpr_write_b32 a58, 0
	v_accvgpr_write_b32 a57, 0
	v_accvgpr_write_b32 a56, 0
	v_accvgpr_write_b32 a55, 0
	v_accvgpr_write_b32 a54, 0
	v_accvgpr_write_b32 a53, 0
	v_accvgpr_write_b32 a52, 0
	v_accvgpr_write_b32 a51, 0
	v_accvgpr_write_b32 a50, 0
	v_accvgpr_write_b32 a49, 0
	v_accvgpr_write_b32 a48, 0
	v_accvgpr_write_b32 a47, 0
	v_accvgpr_write_b32 a46, 0
	v_accvgpr_write_b32 a45, 0
	v_accvgpr_write_b32 a44, 0
	v_accvgpr_write_b32 a43, 0
	v_accvgpr_write_b32 a42, 0
	v_accvgpr_write_b32 a41, 0
	v_accvgpr_write_b32 a40, 0
	v_accvgpr_write_b32 a39, 0
	v_accvgpr_write_b32 a38, 0
	v_accvgpr_write_b32 a37, 0
	v_accvgpr_write_b32 a36, 0
	v_accvgpr_write_b32 a35, 0
	v_accvgpr_write_b32 a34, 0
	v_accvgpr_write_b32 a33, 0
	v_accvgpr_write_b32 a32, 0
	v_accvgpr_write_b32 a31, 0
	v_accvgpr_write_b32 a30, 0
	v_accvgpr_write_b32 a29, 0
	v_accvgpr_write_b32 a28, 0
	v_accvgpr_write_b32 a27, 0
	v_accvgpr_write_b32 a26, 0
	v_accvgpr_write_b32 a25, 0
	v_accvgpr_write_b32 a24, 0
	v_accvgpr_write_b32 a23, 0
	v_accvgpr_write_b32 a22, 0
	v_accvgpr_write_b32 a21, 0
	v_accvgpr_write_b32 a20, 0
	v_accvgpr_write_b32 a19, 0
	v_accvgpr_write_b32 a18, 0
	v_accvgpr_write_b32 a17, 0
	v_accvgpr_write_b32 a16, 0
	v_accvgpr_write_b32 a15, 0
	v_accvgpr_write_b32 a14, 0
	v_accvgpr_write_b32 a13, 0
	v_accvgpr_write_b32 a12, 0
	v_accvgpr_write_b32 a11, 0
	v_accvgpr_write_b32 a10, 0
	v_accvgpr_write_b32 a9, 0
	v_accvgpr_write_b32 a8, 0
	v_accvgpr_write_b32 a7, 0
	v_accvgpr_write_b32 a6, 0
	v_accvgpr_write_b32 a5, 0
	v_accvgpr_write_b32 a4, 0
	v_accvgpr_write_b32 a3, 0
	v_accvgpr_write_b32 a2, 0
	v_accvgpr_write_b32 a1, 0
	v_accvgpr_write_b32 a0, 0
	s_waitcnt lgkmcnt(0)
	s_mov_b64 s[14:15], s[4:5]
	v_add_u32_e32 v88, v8, v2
	v_lshl_or_b32 v4, v1, 3, v12
	v_mul_hi_u32_u24_e32 v9, 0x190, v4
	v_mul_u32_u24_e32 v8, 0x190, v4
	v_mov_b32_e32 v4, 0xd1c40
	v_mad_i64_i32 v[8:9], s[0:1], s12, v4, v[8:9]
	v_lshlrev_b32_e32 v4, 2, v13
	v_lshl_add_u64 v[4:5], v[8:9], 0, v[4:5]
	v_lshl_add_u64 v[4:5], s[6:7], 0, v[4:5]
	s_mov_b32 s4, 32
	s_mov_b64 s[0:1], 0
	s_movk_i32 s5, 0x1000
	s_movk_i32 s6, 0x2000
	s_mov_b32 s7, 0
.LBB3_2:
	v_lshl_add_u64 v[40:41], v[4:5], 0, s[0:1]
	global_load_dwordx4 v[8:11], v[40:41], off nt
	global_load_dwordx4 v[12:15], v[40:41], off offset:400 nt
	global_load_dwordx4 v[16:19], v[40:41], off offset:800 nt
	global_load_dwordx4 v[20:23], v[40:41], off offset:1200 nt
	global_load_dwordx4 v[24:27], v[40:41], off offset:1600 nt
	global_load_dwordx4 v[28:31], v[40:41], off offset:2000 nt
	global_load_dwordx4 v[32:35], v[40:41], off offset:2400 nt
	global_load_dwordx4 v[36:39], v[40:41], off offset:2800 nt
	v_add_co_u32_e32 v56, vcc, s5, v40
	s_nop 1
	v_addc_co_u32_e32 v57, vcc, 0, v41, vcc
	v_add_co_u32_e32 v68, vcc, s6, v40
	s_nop 1
	v_addc_co_u32_e32 v69, vcc, 0, v41, vcc
	global_load_dwordx4 v[40:43], v[56:57], off offset:2304 nt
	global_load_dwordx4 v[44:47], v[56:57], off offset:2704 nt
	global_load_dwordx4 v[48:51], v[56:57], off offset:3104 nt
	global_load_dwordx4 v[52:55], v[56:57], off offset:3504 nt
	s_nop 0
	global_load_dwordx4 v[56:59], v[56:57], off offset:3904 nt
	s_nop 0
	global_load_dwordx4 v[60:63], v[68:69], off offset:208 nt
	global_load_dwordx4 v[64:67], v[68:69], off offset:608 nt
	s_nop 0
	global_load_dwordx4 v[68:71], v[68:69], off offset:1008 nt
	s_and_b32 s2, s7, 0x4000
	s_sub_i32 s12, s4, 32
	s_and_b32 s12, s12, 64
	s_add_u32 s12, s12, s2
	s_and_b32 s13, s4, 0x60
	s_add_u32 s13, s13, s2
	s_waitcnt vmcnt(16)
	v_lshrrev_b32_e32 v90, 7, v89
	v_lshlrev_b32_e32 v90, 19, v90
	v_lshlrev_b32_e32 v91, 7, v89
	v_and_b32_e32 v91, 0x3f80, v91
	v_add3_u32 v90, v90, v91, v88
	v_add_u32_e32 v72, s12, v90
	v_add_u32_e32 v76, s13, v90
	global_load_dwordx4 v[72:75], v72, s[14:15]
	global_load_dwordx4 v[76:79], v76, s[14:15]
	s_add_i32 s4, s4, 64
	s_add_u32 s0, s0, 0x3200
	s_addc_u32 s1, s1, 0
	s_addk_i32 s7, 0x2000
	s_cmpk_eq_u32 s0, 0xc800
	s_waitcnt vmcnt(16)
	v_cvt_pk_f16_f32 v80, v8, v12
	s_waitcnt vmcnt(14)
	v_cvt_pk_f16_f32 v81, v16, v20
	v_cvt_pk_f16_f32 v19, v19, v23
	s_waitcnt vmcnt(12)
	v_cvt_pk_f16_f32 v82, v24, v28
	v_cvt_pk_f16_f32 v84, v25, v29
	s_waitcnt vmcnt(10)
	v_cvt_pk_f16_f32 v83, v32, v36
	v_cvt_pk_f16_f32 v85, v33, v37
	v_cvt_pk_f16_f32 v87, v34, v38
	v_cvt_pk_f16_f32 v86, v26, v30
	v_cvt_pk_f16_f32 v20, v27, v31
	s_waitcnt vmcnt(1)
	v_mfma_f32_32x32x16_f16 a[0:15], v[80:83], v[72:75], a[0:15]
	v_cvt_pk_f16_f32 v83, v17, v21
	v_cvt_pk_f16_f32 v82, v9, v13
	v_cvt_pk_f16_f32 v9, v48, v52
	v_cvt_pk_f16_f32 v8, v40, v44
	v_cvt_pk_f16_f32 v21, v35, v39
	v_cvt_pk_f16_f32 v13, v65, v69
	v_cvt_pk_f16_f32 v12, v57, v61
	v_mfma_f32_32x32x16_f16 a[16:31], v[82:85], v[72:75], a[16:31]
	v_cvt_pk_f16_f32 v85, v18, v22
	v_cvt_pk_f16_f32 v84, v10, v14
	v_cvt_pk_f16_f32 v18, v11, v15
	v_cvt_pk_f16_f32 v11, v64, v68
	v_cvt_pk_f16_f32 v10, v56, v60
	v_cvt_pk_f16_f32 v15, v66, v70
	v_cvt_pk_f16_f32 v14, v58, v62
	s_waitcnt vmcnt(0)
	v_mfma_f32_32x32x16_f16 a[0:15], v[8:11], v[76:79], a[0:15]
	v_cvt_pk_f16_f32 v11, v49, v53
	v_cvt_pk_f16_f32 v10, v41, v45
	v_cvt_pk_f16_f32 v9, v51, v55
	v_cvt_pk_f16_f32 v8, v43, v47
	v_mfma_f32_32x32x16_f16 a[32:47], v[84:87], v[72:75], a[32:47]
	v_mfma_f32_32x32x16_f16 a[48:63], v[18:21], v[72:75], a[48:63]
	v_mfma_f32_32x32x16_f16 a[16:31], v[10:13], v[76:79], a[16:31]
	v_cvt_pk_f16_f32 v13, v50, v54
	v_cvt_pk_f16_f32 v12, v42, v46
	v_cvt_pk_f16_f32 v11, v67, v71
	v_cvt_pk_f16_f32 v10, v59, v63
	v_mfma_f32_32x32x16_f16 a[32:47], v[12:15], v[76:79], a[32:47]
	s_nop 0
	v_mfma_f32_32x32x16_f16 a[48:63], v[8:11], v[76:79], a[48:63]
	s_cbranch_scc0 .LBB3_2
	v_mul_u32_u24_e32 v2, 0x190, v6
	s_movk_i32 s0, 0x3200
	v_mad_u32_u24 v2, v7, s0, v2
	v_lshl_add_u32 v3, v1, 6, v2
	s_nop 6
	v_accvgpr_mov_b32 a63, a16
	v_accvgpr_mov_b32 a14, a1
	v_accvgpr_mov_b32 a15, a17
	v_accvgpr_mov_b32 a16, a33
	v_accvgpr_mov_b32 a17, a49
	v_accvgpr_mov_b32 a65, a48
	ds_write_b128 v3, a[14:17] offset:16
	v_accvgpr_mov_b32 a17, a50
	v_accvgpr_mov_b32 a48, a3
	v_accvgpr_mov_b32 a49, a19
	v_accvgpr_mov_b32 a50, a35
	v_accvgpr_mov_b32 a62, a0
	v_accvgpr_mov_b32 a14, a2
	ds_write_b128 v3, a[48:51] offset:48
	v_accvgpr_mov_b32 a0, a4
	v_accvgpr_mov_b32 a1, a20
	v_accvgpr_mov_b32 a2, a36
	v_accvgpr_mov_b32 a3, a52
	v_accvgpr_mov_b32 a50, a5
	v_accvgpr_mov_b32 a51, a21
	v_accvgpr_mov_b32 a52, a37
	ds_write_b128 v3, a[0:3] offset:128
	ds_write_b128 v3, a[50:53] offset:144
	v_accvgpr_mov_b32 a0, a6
	v_accvgpr_mov_b32 a1, a22
	v_accvgpr_mov_b32 a2, a38
	v_accvgpr_mov_b32 a3, a54
	v_accvgpr_mov_b32 a52, a7
	v_accvgpr_mov_b32 a53, a23
	v_accvgpr_mov_b32 a54, a39
	ds_write_b128 v3, a[0:3] offset:160
	ds_write_b128 v3, a[52:55] offset:176
	v_accvgpr_mov_b32 a0, a8
	v_accvgpr_mov_b32 a1, a24
	v_accvgpr_mov_b32 a2, a40
	v_accvgpr_mov_b32 a3, a56
	v_accvgpr_mov_b32 a54, a9
	v_accvgpr_mov_b32 a55, a25
	v_accvgpr_mov_b32 a56, a41
	v_accvgpr_mov_b32 a64, a32
	v_accvgpr_mov_b32 a15, a18
	v_accvgpr_mov_b32 a16, a34
	ds_write_b128 v3, a[0:3] offset:256
	ds_write_b128 v3, a[54:57] offset:272
	v_accvgpr_mov_b32 a0, a10
	v_accvgpr_mov_b32 a1, a26
	v_accvgpr_mov_b32 a2, a42
	v_accvgpr_mov_b32 a3, a58
	v_accvgpr_mov_b32 a56, a11
	v_accvgpr_mov_b32 a57, a27
	v_accvgpr_mov_b32 a58, a43
	v_cmp_eq_u32_e32 vcc, 0, v1
	ds_write_b128 v3, a[62:65]
	ds_write_b128 v3, a[14:17] offset:32
	ds_write_b128 v3, a[0:3] offset:288
	ds_write_b128 v3, a[56:59] offset:304
	s_and_saveexec_b64 s[0:1], vcc
	v_accvgpr_mov_b32 a13, a28
	v_accvgpr_mov_b32 a14, a44
	v_accvgpr_mov_b32 a15, a60
	ds_write_b128 v2, a[12:15] offset:384
	s_or_b64 exec, exec, s[0:1]
	s_movk_i32 s0, 0x320
	v_cmp_gt_u32_e32 vcc, s0, v0
	s_waitcnt lgkmcnt(0)
	s_barrier
	s_and_saveexec_b64 s[0:1], vcc
	s_cbranch_execz .LBB3_8
	s_mul_i32 s1, s8, 0xc800
	s_mulk_i32 s9, 0x3200
	s_mul_hi_u32 s0, s8, 0xc800
	s_add_u32 s1, s1, s9
	s_addc_u32 s2, s0, 0
	s_add_u32 s0, s10, s1
	v_or_b32_e32 v4, 0xffffff00, v0
	v_lshlrev_b32_e32 v0, 4, v0
	v_mov_b32_e32 v1, 0
	s_addc_u32 s1, s11, s2
	v_lshl_add_u64 v[2:3], s[0:1], 0, v[0:1]
	s_mov_b64 s[0:1], 0
	s_mov_b32 s2, 0x3d000000
	s_mov_b64 s[4:5], 0x1000
	s_movk_i32 s3, 0x21f

	.amdhsa_kernel _Z13expert_kernelPKcPKfPKiPK15HIP_vector_typeIiLj4EES4_Pf
		.amdhsa_group_segment_fixed_size 51200
		.amdhsa_private_segment_fixed_size 0
		.amdhsa_kernarg_size 48
		.amdhsa_user_sgpr_count 2
		.amdhsa_user_sgpr_dispatch_ptr 0
		.amdhsa_user_sgpr_queue_ptr 0
		.amdhsa_user_sgpr_kernarg_segment_ptr 1
		.amdhsa_user_sgpr_dispatch_id 0
		.amdhsa_user_sgpr_kernarg_preload_length 0
		.amdhsa_user_sgpr_kernarg_preload_offset 0
		.amdhsa_user_sgpr_private_segment_size 0
		.amdhsa_uses_dynamic_stack 0
		.amdhsa_enable_private_segment 0
		.amdhsa_system_sgpr_workgroup_id_x 1
		.amdhsa_system_sgpr_workgroup_id_y 0
		.amdhsa_system_sgpr_workgroup_id_z 0
		.amdhsa_system_sgpr_workgroup_info 0
		.amdhsa_system_vgpr_workitem_id 0
		.amdhsa_next_free_vgpr 158
		.amdhsa_next_free_sgpr 96
		.amdhsa_accum_offset 92
		.amdhsa_reserve_vcc 1
		.amdhsa_float_round_mode_32 0
		.amdhsa_float_round_mode_16_64 0
		.amdhsa_float_denorm_mode_32 3
		.amdhsa_float_denorm_mode_16_64 3
		.amdhsa_dx10_clamp 1
		.amdhsa_ieee_mode 1
		.amdhsa_fp16_overflow 0
		.amdhsa_tg_split 0
		.amdhsa_exception_fp_ieee_invalid_op 0
		.amdhsa_exception_fp_denorm_src 0
		.amdhsa_exception_fp_ieee_div_zero 0
		.amdhsa_exception_fp_ieee_overflow 0
		.amdhsa_exception_fp_ieee_underflow 0
		.amdhsa_exception_fp_ieee_inexact 0
		.amdhsa_exception_int_div_zero 0
	.end_amdhsa_kernel

amdhsa.kernels:
  - .agpr_count:     0
    .args:
      - .actual_access:  read_only
        .address_space:  global
        .offset:         0
        .size:           8
        .value_kind:     global_buffer
      - .actual_access:  write_only
        .address_space:  global
        .offset:         8
        .size:           8
        .value_kind:     global_buffer
      - .actual_access:  read_only
        .address_space:  global
        .offset:         16
        .size:           8
        .value_kind:     global_buffer
      - .actual_access:  read_only
        .address_space:  global
        .offset:         24
        .size:           8
        .value_kind:     global_buffer
      - .actual_access:  read_only
        .address_space:  global
        .offset:         32
        .size:           8
        .value_kind:     global_buffer
      - .actual_access:  write_only
        .address_space:  global
        .offset:         40
        .size:           8
        .value_kind:     global_buffer
      - .actual_access:  write_only
        .address_space:  global
        .offset:         48
        .size:           8
        .value_kind:     global_buffer
      - .actual_access:  write_only
        .address_space:  global
        .offset:         56
        .size:           8
        .value_kind:     global_buffer
      - .actual_access:  write_only
        .address_space:  global
        .offset:         64
        .size:           8
        .value_kind:     global_buffer
      - .actual_access:  write_only
        .address_space:  global
        .offset:         72
        .size:           8
        .value_kind:     global_buffer
      - .actual_access:  write_only
        .address_space:  global
        .offset:         80
        .size:           8
        .value_kind:     global_buffer
    .group_segment_fixed_size: 16640
    .kernarg_segment_align: 8
    .kernarg_segment_size: 88
    .language:       OpenCL C
    .language_version:
      - 2
      - 0
    .max_flat_workgroup_size: 256
    .name:           _Z8prep_allPKfPcS0_S0_S0_S1_S1_S1_PyPiS3_
    .private_segment_fixed_size: 0
    .sgpr_count:     30
    .sgpr_spill_count: 0
    .symbol:         _Z8prep_allPKfPcS0_S0_S0_S1_S1_S1_PyPiS3_.kd
    .uniform_work_group_size: 1
    .uses_dynamic_stack: false
    .vgpr_count:     48
    .vgpr_spill_count: 0
    .wavefront_size: 64
  - .agpr_count:     0
    .args:
      - .actual_access:  read_only
        .address_space:  global
        .offset:         0
        .size:           8
        .value_kind:     global_buffer
      - .actual_access:  write_only
        .address_space:  global
        .offset:         8
        .size:           8
        .value_kind:     global_buffer
      - .actual_access:  write_only
        .address_space:  global
        .offset:         16
        .size:           8
        .value_kind:     global_buffer
      - .address_space:  global
        .offset:         24
        .size:           8
        .value_kind:     global_buffer
    .group_segment_fixed_size: 0
    .kernarg_segment_align: 8
    .kernarg_segment_size: 32
    .language:       OpenCL C
    .language_version:
      - 2
      - 0
    .max_flat_workgroup_size: 256
    .name:           _Z13select_kernelPKfPyPiS2_
    .private_segment_fixed_size: 0
    .sgpr_count:     21
    .sgpr_spill_count: 0
    .symbol:         _Z13select_kernelPKfPyPiS2_.kd
    .uniform_work_group_size: 1
    .uses_dynamic_stack: false
    .vgpr_count:     16
    .vgpr_spill_count: 0
    .wavefront_size: 64
  - .agpr_count:     0
    .args:
      - .actual_access:  read_only
        .address_space:  global
        .offset:         0
        .size:           8
        .value_kind:     global_buffer
      - .actual_access:  write_only
        .address_space:  global
        .offset:         8
        .size:           8
        .value_kind:     global_buffer
      - .actual_access:  write_only
        .address_space:  global
        .offset:         16
        .size:           8
        .value_kind:     global_buffer
      - .actual_access:  write_only
        .address_space:  global
        .offset:         24
        .size:           8
        .value_kind:     global_buffer
    .group_segment_fixed_size: 4128
    .kernarg_segment_align: 8
    .kernarg_segment_size: 32
    .language:       OpenCL C
    .language_version:
      - 2
      - 0
    .max_flat_workgroup_size: 1024
    .name:           _Z12route_kernelPKyPiP15HIP_vector_typeIiLj4EES1_
    .private_segment_fixed_size: 0
    .sgpr_count:     19
    .sgpr_spill_count: 0
    .symbol:         _Z12route_kernelPKyPiP15HIP_vector_typeIiLj4EES1_.kd
    .uniform_work_group_size: 1
    .uses_dynamic_stack: false
    .vgpr_count:     23
    .vgpr_spill_count: 0
    .wavefront_size: 64
  - .agpr_count:     66
    .args:
      - .actual_access:  read_only
        .address_space:  global
        .offset:         0
        .size:           8
        .value_kind:     global_buffer
      - .actual_access:  read_only
        .address_space:  global
        .offset:         8
        .size:           8
        .value_kind:     global_buffer
      - .actual_access:  read_only
        .address_space:  global
        .offset:         16
        .size:           8
        .value_kind:     global_buffer
      - .actual_access:  read_only
        .address_space:  global
        .offset:         24
        .size:           8
        .value_kind:     global_buffer
      - .actual_access:  read_only
        .address_space:  global
        .offset:         32
        .size:           8
        .value_kind:     global_buffer
      - .actual_access:  write_only
        .address_space:  global
        .offset:         40
        .size:           8
        .value_kind:     global_buffer
    .group_segment_fixed_size: 51200
    .kernarg_segment_align: 8
    .kernarg_segment_size: 48
    .language:       OpenCL C
    .language_version:
      - 2
      - 0
    .max_flat_workgroup_size: 256
    .name:           _Z13expert_kernelPKcPKfPKiPK15HIP_vector_typeIiLj4EES4_Pf
    .private_segment_fixed_size: 0
    .sgpr_count:     20
    .sgpr_spill_count: 0
    .symbol:         _Z13expert_kernelPKcPKfPKiPK15HIP_vector_typeIiLj4EES4_Pf.kd
    .uniform_work_group_size: 1
    .uses_dynamic_stack: false
    .vgpr_count:     158
    .vgpr_spill_count: 0
    .wavefront_size: 64
  - .agpr_count:     0
    .args:
      - .actual_access:  read_only
        .address_space:  global
        .offset:         0
        .size:           8
        .value_kind:     global_buffer
      - .actual_access:  read_only
        .address_space:  global
        .offset:         8
        .size:           8
        .value_kind:     global_buffer
      - .actual_access:  read_only
        .address_space:  global
        .offset:         16
        .size:           8
        .value_kind:     global_buffer
      - .actual_access:  read_only
        .address_space:  global
        .offset:         24
        .size:           8
        .value_kind:     global_buffer
      - .actual_access:  read_only
        .address_space:  global
        .offset:         32
        .size:           8
        .value_kind:     global_buffer
      - .actual_access:  read_only
        .address_space:  global
        .offset:         40
        .size:           8
        .value_kind:     global_buffer
      - .actual_access:  read_only
        .address_space:  global
        .offset:         48
        .size:           8
        .value_kind:     global_buffer
      - .actual_access:  read_only
        .address_space:  global
        .offset:         56
        .size:           8
        .value_kind:     global_buffer
      - .actual_access:  read_only
        .address_space:  global
        .offset:         64
        .size:           8
        .value_kind:     global_buffer
      - .actual_access:  write_only
        .address_space:  global
        .offset:         72
        .size:           8
        .value_kind:     global_buffer
    .group_segment_fixed_size: 14000
    .kernarg_segment_align: 8
    .kernarg_segment_size: 80
    .language:       OpenCL C
    .language_version:
      - 2
      - 0
    .max_flat_workgroup_size: 256
    .name:           _Z12final_kernelPKfPKiPK15HIP_vector_typeIiLj4EES2_S2_S0_S0_S0_S0_Pf
    .private_segment_fixed_size: 0
    .sgpr_count:     50
    .sgpr_spill_count: 0
    .symbol:         _Z12final_kernelPKfPKiPK15HIP_vector_typeIiLj4EES2_S2_S0_S0_S0_S0_Pf.kd
    .uniform_work_group_size: 1
    .uses_dynamic_stack: false
    .vgpr_count:     140
    .vgpr_spill_count: 0
    .wavefront_size: 64
  - .agpr_count:     0
    .args:
      - .address_space:  global
        .offset:         0
        .size:           8
        .value_kind:     global_buffer
      - .address_space:  global
        .offset:         8
        .size:           8
        .value_kind:     global_buffer
      - .offset:         16
        .size:           4
        .value_kind:     by_value
      - .offset:         20
        .size:           4
        .value_kind:     by_value
      - .actual_access:  read_only
        .address_space:  global
        .offset:         24
        .size:           8
        .value_kind:     global_buffer
      - .offset:         32
        .size:           4
        .value_kind:     by_value
      - .actual_access:  read_only
        .address_space:  global
        .offset:         40
        .size:           8
        .value_kind:     global_buffer
      - .actual_access:  read_only
        .address_space:  global
        .offset:         48
        .size:           8
        .value_kind:     global_buffer
      - .actual_access:  write_only
        .address_space:  global
        .offset:         56
        .size:           8
        .value_kind:     global_buffer
      - .offset:         64
        .size:           4
        .value_kind:     by_value
      - .actual_access:  read_only
        .address_space:  global
        .offset:         72
        .size:           8
        .value_kind:     global_buffer
    .group_segment_fixed_size: 0
    .kernarg_segment_align: 8
    .kernarg_segment_size: 80
    .language:       OpenCL C
    .language_version:
      - 2
      - 0
    .max_flat_workgroup_size: 512
    .name:           _Z7gemm_x3ILi2ELi2ELi2ELi0EEvPKcS1_iiPKfiS3_PKiPciPy
    .private_segment_fixed_size: 0
    .sgpr_count:     38
    .sgpr_spill_count: 0
    .symbol:         _Z7gemm_x3ILi2ELi2ELi2ELi0EEvPKcS1_iiPKfiS3_PKiPciPy.kd
    .uniform_work_group_size: 1
    .uses_dynamic_stack: false
    .vgpr_count:     208
    .vgpr_spill_count: 0
    .wavefront_size: 64
  - .agpr_count:     0
    .args:
      - .address_space:  global
        .offset:         0
        .size:           8
        .value_kind:     global_buffer
      - .address_space:  global
        .offset:         8
        .size:           8
        .value_kind:     global_buffer
      - .offset:         16
        .size:           4
        .value_kind:     by_value
      - .offset:         20
        .size:           4
        .value_kind:     by_value
      - .actual_access:  read_only
        .address_space:  global
        .offset:         24
        .size:           8
        .value_kind:     global_buffer
      - .offset:         32
        .size:           4
        .value_kind:     by_value
      - .actual_access:  read_only
        .address_space:  global
        .offset:         40
        .size:           8
        .value_kind:     global_buffer
      - .actual_access:  read_only
        .address_space:  global
        .offset:         48
        .size:           8
        .value_kind:     global_buffer
      - .actual_access:  write_only
        .address_space:  global
        .offset:         56
        .size:           8
        .value_kind:     global_buffer
      - .offset:         64
        .size:           4
        .value_kind:     by_value
      - .actual_access:  read_only
        .address_space:  global
        .offset:         72
        .size:           8
        .value_kind:     global_buffer
    .group_segment_fixed_size: 0
    .kernarg_segment_align: 8
    .kernarg_segment_size: 80
    .language:       OpenCL C
    .language_version:
      - 2
      - 0
    .max_flat_workgroup_size: 512
    .name:           _Z7gemm_x3ILi2ELi2ELi1ELi1EEvPKcS1_iiPKfiS3_PKiPciPy
    .private_segment_fixed_size: 0
    .sgpr_count:     32
    .sgpr_spill_count: 0
    .symbol:         _Z7gemm_x3ILi2ELi2ELi1ELi1EEvPKcS1_iiPKfiS3_PKiPciPy.kd
    .uniform_work_group_size: 1
    .uses_dynamic_stack: false
    .vgpr_count:     114
    .vgpr_spill_count: 0
    .wavefront_size: 64
  - .agpr_count:     32
    .args:
      - .address_space:  global
        .offset:         0
        .size:           8
        .value_kind:     global_buffer
      - .address_space:  global
        .offset:         8
        .size:           8
        .value_kind:     global_buffer
      - .offset:         16
        .size:           4
        .value_kind:     by_value
      - .offset:         20
        .size:           4
        .value_kind:     by_value
      - .actual_access:  read_only
        .address_space:  global
        .offset:         24
        .size:           8
        .value_kind:     global_buffer
      - .offset:         32
        .size:           4
        .value_kind:     by_value
      - .actual_access:  read_only
        .address_space:  global
        .offset:         40
        .size:           8
        .value_kind:     global_buffer
      - .actual_access:  read_only
        .address_space:  global
        .offset:         48
        .size:           8
        .value_kind:     global_buffer
      - .actual_access:  write_only
        .address_space:  global
        .offset:         56
        .size:           8
        .value_kind:     global_buffer
      - .offset:         64
        .size:           4
        .value_kind:     by_value
      - .address_space:  global
        .offset:         72
        .size:           8
        .value_kind:     global_buffer
    .group_segment_fixed_size: 0
    .kernarg_segment_align: 8
    .kernarg_segment_size: 80
    .language:       OpenCL C
    .language_version:
      - 2
      - 0
    .max_flat_workgroup_size: 256
    .name:           _Z7gemm_x3ILi1ELi2ELi1ELi2EEvPKcS1_iiPKfiS3_PKiPciPy
    .private_segment_fixed_size: 0
    .sgpr_count:     29
    .sgpr_spill_count: 0
    .symbol:         _Z7gemm_x3ILi1ELi2ELi1ELi2EEvPKcS1_iiPKfiS3_PKiPciPy.kd
    .uniform_work_group_size: 1
    .uses_dynamic_stack: false
    .vgpr_count:     136
    .vgpr_spill_count: 0
    .wavefront_size: 64
  - .agpr_count:     0
    .args:
      - .actual_access:  read_only
        .address_space:  global
        .offset:         0
        .size:           8
        .value_kind:     global_buffer
      - .offset:         8
        .size:           4
        .value_kind:     by_value
      - .offset:         12
        .size:           4
        .value_kind:     by_value
      - .actual_access:  read_only
        .address_space:  global
        .offset:         16
        .size:           8
        .value_kind:     global_buffer
      - .offset:         24
        .size:           4
        .value_kind:     by_value
      - .offset:         28
        .size:           4
        .value_kind:     by_value
      - .actual_access:  read_only
        .address_space:  global
        .offset:         32
        .size:           8
        .value_kind:     global_buffer
      - .actual_access:  read_only
        .address_space:  global
        .offset:         40
        .size:           8
        .value_kind:     global_buffer
      - .actual_access:  read_only
        .address_space:  global
        .offset:         48
        .size:           8
        .value_kind:     global_buffer
      - .actual_access:  read_only
        .address_space:  global
        .offset:         56
        .size:           8
        .value_kind:     global_buffer
      - .actual_access:  write_only
        .address_space:  global
        .offset:         64
        .size:           8
        .value_kind:     global_buffer
      - .offset:         72
        .size:           4
        .value_kind:     by_value
      - .actual_access:  read_only
        .address_space:  global
        .offset:         80
        .size:           8
        .value_kind:     global_buffer
      - .offset:         88
        .size:           4
        .value_kind:     hidden_block_count_x
      - .offset:         92
        .size:           4
        .value_kind:     hidden_block_count_y
      - .offset:         96
        .size:           4
        .value_kind:     hidden_block_count_z
      - .offset:         100
        .size:           2
        .value_kind:     hidden_group_size_x
      - .offset:         102
        .size:           2
        .value_kind:     hidden_group_size_y
      - .offset:         104
        .size:           2
        .value_kind:     hidden_group_size_z
      - .offset:         106
        .size:           2
        .value_kind:     hidden_remainder_x
      - .offset:         108
        .size:           2
        .value_kind:     hidden_remainder_y
      - .offset:         110
        .size:           2
        .value_kind:     hidden_remainder_z
      - .offset:         128
        .size:           8
        .value_kind:     hidden_global_offset_x
      - .offset:         136
        .size:           8
        .value_kind:     hidden_global_offset_y
      - .offset:         144
        .size:           8
        .value_kind:     hidden_global_offset_z
      - .offset:         152
        .size:           2
        .value_kind:     hidden_grid_dims
    .group_segment_fixed_size: 16384
    .kernarg_segment_align: 8
    .kernarg_segment_size: 344
    .language:       OpenCL C
    .language_version:
      - 2
      - 0
    .max_flat_workgroup_size: 1024
    .name:           _Z13refine_kernelILi1ELi16ELi128ELb1ELi4EEvPKfiiS1_iiS1_PKiS3_S3_PfiPy
    .private_segment_fixed_size: 0
    .sgpr_count:     35
    .sgpr_spill_count: 0
    .symbol:         _Z13refine_kernelILi1ELi16ELi128ELb1ELi4EEvPKfiiS1_iiS1_PKiS3_S3_PfiPy.kd
    .uniform_work_group_size: 1
    .uses_dynamic_stack: false
    .vgpr_count:     64
    .vgpr_spill_count: 0
    .wavefront_size: 64
  - .agpr_count:     0
    .args:
      - .actual_access:  read_only
        .address_space:  global
        .offset:         0
        .size:           8
        .value_kind:     global_buffer
      - .offset:         8
        .size:           4
        .value_kind:     by_value
      - .offset:         12
        .size:           4
        .value_kind:     by_value
      - .actual_access:  read_only
        .address_space:  global
        .offset:         16
        .size:           8
        .value_kind:     global_buffer
      - .offset:         24
        .size:           4
        .value_kind:     by_value
      - .offset:         28
        .size:           4
        .value_kind:     by_value
      - .actual_access:  read_only
        .address_space:  global
        .offset:         32
        .size:           8
        .value_kind:     global_buffer
      - .actual_access:  read_only
        .address_space:  global
        .offset:         40
        .size:           8
        .value_kind:     global_buffer
      - .actual_access:  read_only
        .address_space:  global
        .offset:         48
        .size:           8
        .value_kind:     global_buffer
      - .actual_access:  read_only
        .address_space:  global
        .offset:         56
        .size:           8
        .value_kind:     global_buffer
      - .actual_access:  write_only
        .address_space:  global
        .offset:         64
        .size:           8
        .value_kind:     global_buffer
      - .offset:         72
        .size:           4
        .value_kind:     by_value
      - .actual_access:  read_only
        .address_space:  global
        .offset:         80
        .size:           8
        .value_kind:     global_buffer
      - .offset:         88
        .size:           4
        .value_kind:     hidden_block_count_x
      - .offset:         92
        .size:           4
        .value_kind:     hidden_block_count_y
      - .offset:         96
        .size:           4
        .value_kind:     hidden_block_count_z
      - .offset:         100
        .size:           2
        .value_kind:     hidden_group_size_x
      - .offset:         102
        .size:           2
        .value_kind:     hidden_group_size_y
      - .offset:         104
        .size:           2
        .value_kind:     hidden_group_size_z
      - .offset:         106
        .size:           2
        .value_kind:     hidden_remainder_x
      - .offset:         108
        .size:           2
        .value_kind:     hidden_remainder_y
      - .offset:         110
        .size:           2
        .value_kind:     hidden_remainder_z
      - .offset:         128
        .size:           8
        .value_kind:     hidden_global_offset_x
      - .offset:         136
        .size:           8
        .value_kind:     hidden_global_offset_y
      - .offset:         144
        .size:           8
        .value_kind:     hidden_global_offset_z
      - .offset:         152
        .size:           2
        .value_kind:     hidden_grid_dims
    .group_segment_fixed_size: 16384
    .kernarg_segment_align: 8
    .kernarg_segment_size: 344
    .language:       OpenCL C
    .language_version:
      - 2
      - 0
    .max_flat_workgroup_size: 1024
    .name:           _Z13refine_kernelILi2ELi16ELi64ELb0ELi4EEvPKfiiS1_iiS1_PKiS3_S3_PfiPy
    .private_segment_fixed_size: 0
    .sgpr_count:     35
    .sgpr_spill_count: 0
    .symbol:         _Z13refine_kernelILi2ELi16ELi64ELb0ELi4EEvPKfiiS1_iiS1_PKiS3_S3_PfiPy.kd
    .uniform_work_group_size: 1
    .uses_dynamic_stack: false
    .vgpr_count:     85
    .vgpr_spill_count: 0
    .wavefront_size: 64
  - .agpr_count:     0
    .args:
      - .actual_access:  read_only
        .address_space:  global
        .offset:         0
        .size:           8
        .value_kind:     global_buffer
      - .offset:         8
        .size:           4
        .value_kind:     by_value
      - .offset:         12
        .size:           4
        .value_kind:     by_value
      - .actual_access:  read_only
        .address_space:  global
        .offset:         16
        .size:           8
        .value_kind:     global_buffer
      - .offset:         24
        .size:           4
        .value_kind:     by_value
      - .offset:         28
        .size:           4
        .value_kind:     by_value
      - .actual_access:  read_only
        .address_space:  global
        .offset:         32
        .size:           8
        .value_kind:     global_buffer
      - .actual_access:  read_only
        .address_space:  global
        .offset:         40
        .size:           8
        .value_kind:     global_buffer
      - .actual_access:  read_only
        .address_space:  global
        .offset:         48
        .size:           8
        .value_kind:     global_buffer
      - .actual_access:  read_only
        .address_space:  global
        .offset:         56
        .size:           8
        .value_kind:     global_buffer
      - .actual_access:  read_only
        .address_space:  global
        .offset:         64
        .size:           8
        .value_kind:     global_buffer
      - .offset:         72
        .size:           4
        .value_kind:     by_value
      - .address_space:  global
        .offset:         80
        .size:           8
        .value_kind:     global_buffer
      - .offset:         88
        .size:           4
        .value_kind:     hidden_block_count_x
      - .offset:         92
        .size:           4
        .value_kind:     hidden_block_count_y
      - .offset:         96
        .size:           4
        .value_kind:     hidden_block_count_z
      - .offset:         100
        .size:           2
        .value_kind:     hidden_group_size_x
      - .offset:         102
        .size:           2
        .value_kind:     hidden_group_size_y
      - .offset:         104
        .size:           2
        .value_kind:     hidden_group_size_z
      - .offset:         106
        .size:           2
        .value_kind:     hidden_remainder_x
      - .offset:         108
        .size:           2
        .value_kind:     hidden_remainder_y
      - .offset:         110
        .size:           2
        .value_kind:     hidden_remainder_z
      - .offset:         128
        .size:           8
        .value_kind:     hidden_global_offset_x
      - .offset:         136
        .size:           8
        .value_kind:     hidden_global_offset_y
      - .offset:         144
        .size:           8
        .value_kind:     hidden_global_offset_z
      - .offset:         152
        .size:           2
        .value_kind:     hidden_grid_dims
    .group_segment_fixed_size: 8192
    .kernarg_segment_align: 8
    .kernarg_segment_size: 344
    .language:       OpenCL C
    .language_version:
      - 2
      - 0
    .max_flat_workgroup_size: 512
    .name:           _Z13refine_kernelILi3ELi8ELi64ELb0ELi4EEvPKfiiS1_iiS1_PKiS3_S3_PfiPy
    .private_segment_fixed_size: 0
    .sgpr_count:     38
    .sgpr_spill_count: 0
    .symbol:         _Z13refine_kernelILi3ELi8ELi64ELb0ELi4EEvPKfiiS1_iiS1_PKiS3_S3_PfiPy.kd
    .uniform_work_group_size: 1
    .uses_dynamic_stack: false
    .vgpr_count:     88
    .vgpr_spill_count: 0
    .wavefront_size: 64
